# MoE up-GEMM epilogue: 2^-18 scale folded into the sigmoid denominator (one VALU less per element); on top of v34
# baseline (speedup 1.0000x reference)
.LBB0_1830:
	s_mov_b32 s94, 0x48800000
	v_mov_b32_e32 v2, 0
	v_readlane_b32 s2, v254, 10
	s_lshl_b32 s2, s2, 8
	v_add_u32_e32 v3, v2, v187
	v_add3_u32 v2, s2, v188, v2
	v_readlane_b32 s2, v254, 11
	s_lshl_b32 s2, s2, 7
	s_or_b32 s2, s2, s52
	v_lshl_add_u32 v4, v3, 3, s2
	v_mul_f32_e32 v3, 0xbab8aa3b, v170
	v_exp_f32_e32 v3, v3
	v_mul_f32_e32 v7, 0xbab8aa3b, v162
	v_exp_f32_e32 v7, v7
	v_mul_f32_e32 v6, v174, v170
	v_fma_f32 v3, v3, s94, s94
	v_rcp_f32_e32 v3, v3
	v_fma_f32 v7, v7, s94, s94
	v_rcp_f32_e32 v7, v7

	v_mul_f32_e32 v3, v6, v3
	v_mul_f32_e32 v6, v166, v162

	v_mul_f32_e32 v7, v6, v7
	v_mul_f32_e32 v6, 0xbab8aa3b, v171
	v_exp_f32_e32 v6, v6
	v_mul_f32_e32 v9, 0xbab8aa3b, v163
	v_exp_f32_e32 v9, v9
	v_mul_f32_e32 v8, v175, v171
	v_fma_f32 v6, v6, s94, s94
	v_rcp_f32_e32 v6, v6
	v_fma_f32 v9, v9, s94, s94
	v_rcp_f32_e32 v9, v9

	v_mul_f32_e32 v6, v8, v6
	v_mul_f32_e32 v8, v167, v163

	v_mul_f32_e32 v8, v8, v9
	v_mul_f32_e32 v9, 0xbab8aa3b, v172
	v_exp_f32_e32 v9, v9
	v_mul_f32_e32 v11, 0xbab8aa3b, v164
	v_exp_f32_e32 v11, v11
	v_mul_f32_e32 v10, v176, v172
	v_fma_f32 v9, v9, s94, s94
	v_rcp_f32_e32 v9, v9
	v_fma_f32 v11, v11, s94, s94
	v_rcp_f32_e32 v11, v11

	v_mul_f32_e32 v9, v10, v9
	v_mul_f32_e32 v10, v168, v164

	v_mul_f32_e32 v10, v10, v11
	v_mul_f32_e32 v11, 0xbab8aa3b, v173
	v_exp_f32_e32 v11, v11
	v_mul_f32_e32 v13, 0xbab8aa3b, v165
	v_exp_f32_e32 v13, v13
	v_mul_f32_e32 v12, v177, v173
	v_fma_f32 v11, v11, s94, s94
	v_rcp_f32_e32 v11, v11
	v_fma_f32 v13, v13, s94, s94
	v_rcp_f32_e32 v13, v13

	v_mul_f32_e32 v11, v12, v11
	v_mul_f32_e32 v12, v169, v165

	v_mul_f32_e32 v12, v12, v13
	v_med3_f32 v3, v3, s60, v195
	v_med3_f32 v13, v6, s60, v195
	v_mov_b32_e32 v6, 0
	v_cvt_pk_fp8_f32 v6, v3, v13
	v_med3_f32 v3, v7, s60, v195
	v_med3_f32 v8, v8, s60, v195
	v_mov_b32_e32 v7, 0
	v_cvt_pk_fp8_f32 v7, v3, v8
	v_med3_f32 v3, v10, s60, v195
	v_med3_f32 v8, v12, s60, v195
	v_med3_f32 v9, v9, s60, v195
	v_med3_f32 v11, v11, s60, v195
	v_cvt_pk_fp8_f32 v7, v3, v8 op_sel:[0,0,1]
	v_ashrrev_i32_e32 v3, 31, v2
	v_cvt_pk_fp8_f32 v6, v9, v11 op_sel:[0,0,1]
	v_lshlrev_b64 v[2:3], 9, v[2:3]
	v_ashrrev_i32_e32 v5, 31, v4
	v_lshl_add_u64 v[2:3], s[22:23], 0, v[2:3]
	v_lshl_add_u64 v[2:3], v[2:3], 0, v[4:5]
	v_mul_f32_e32 v4, 0xbab8aa3b, v154
	v_exp_f32_e32 v4, v4
	global_store_dwordx2 v[2:3], v[6:7], off
	v_mul_f32_e32 v6, 0xbab8aa3b, v146
	v_exp_f32_e32 v6, v6
	v_fma_f32 v4, v4, s94, s94
	v_rcp_f32_e32 v4, v4
	v_mul_f32_e32 v5, v158, v154
	v_fma_f32 v6, v6, s94, s94
	v_rcp_f32_e32 v6, v6

	v_mul_f32_e32 v4, v5, v4
	v_mul_f32_e32 v5, v150, v146

	v_mul_f32_e32 v5, v5, v6
	v_mul_f32_e32 v6, 0xbab8aa3b, v155
	v_exp_f32_e32 v6, v6
	v_mul_f32_e32 v8, 0xbab8aa3b, v147
	v_exp_f32_e32 v8, v8
	v_mul_f32_e32 v7, v159, v155
	v_fma_f32 v6, v6, s94, s94
	v_rcp_f32_e32 v6, v6
	v_fma_f32 v8, v8, s94, s94
	v_rcp_f32_e32 v8, v8

	v_mul_f32_e32 v6, v7, v6
	v_mul_f32_e32 v7, v151, v147

	v_mul_f32_e32 v7, v7, v8
	v_mul_f32_e32 v8, 0xbab8aa3b, v156
	v_exp_f32_e32 v8, v8
	v_mul_f32_e32 v10, 0xbab8aa3b, v148
	v_exp_f32_e32 v10, v10
	v_mul_f32_e32 v9, v160, v156
	v_fma_f32 v8, v8, s94, s94
	v_rcp_f32_e32 v8, v8
	v_fma_f32 v10, v10, s94, s94
	v_rcp_f32_e32 v10, v10

	v_mul_f32_e32 v8, v9, v8
	v_mul_f32_e32 v9, v152, v148

	v_mul_f32_e32 v9, v9, v10
	v_mul_f32_e32 v10, 0xbab8aa3b, v157
	v_exp_f32_e32 v10, v10
	v_mul_f32_e32 v12, 0xbab8aa3b, v149
	v_exp_f32_e32 v12, v12
	v_mul_f32_e32 v11, v161, v157
	v_fma_f32 v10, v10, s94, s94
	v_rcp_f32_e32 v10, v10
	v_fma_f32 v12, v12, s94, s94
	v_rcp_f32_e32 v12, v12

	v_mul_f32_e32 v10, v11, v10
	v_mul_f32_e32 v11, v153, v149

	v_mul_f32_e32 v11, v11, v12
	v_med3_f32 v12, v4, s60, v195
	v_med3_f32 v6, v6, s60, v195
	v_mov_b32_e32 v4, 0
	v_cvt_pk_fp8_f32 v4, v12, v6
	v_med3_f32 v6, v5, s60, v195
	v_med3_f32 v7, v7, s60, v195
	v_mov_b32_e32 v5, 0
	v_cvt_pk_fp8_f32 v5, v6, v7
	v_med3_f32 v8, v8, s60, v195
	v_med3_f32 v10, v10, s60, v195
	v_med3_f32 v6, v9, s60, v195
	v_med3_f32 v7, v11, s60, v195
	v_cvt_pk_fp8_f32 v4, v8, v10 op_sel:[0,0,1]
	v_cvt_pk_fp8_f32 v5, v6, v7 op_sel:[0,0,1]
	v_add_co_u32_e32 v6, vcc, s45, v2
	v_mul_f32_e32 v8, 0xbab8aa3b, v131
	s_nop 0
	v_addc_co_u32_e32 v7, vcc, 0, v3, vcc
	global_store_dwordx2 v[6:7], v[4:5], off
	v_mul_f32_e32 v4, 0xbab8aa3b, v138
	v_exp_f32_e32 v4, v4
	v_mul_f32_e32 v6, 0xbab8aa3b, v130
	v_exp_f32_e32 v6, v6
	v_mul_f32_e32 v5, v142, v138
	v_fma_f32 v4, v4, s94, s94
	v_rcp_f32_e32 v4, v4
	v_fma_f32 v6, v6, s94, s94
	v_rcp_f32_e32 v6, v6

	v_mul_f32_e32 v4, v5, v4
	v_mul_f32_e32 v5, v134, v130

	v_mul_f32_e32 v5, v5, v6
	v_mul_f32_e32 v6, 0xbab8aa3b, v139
	v_exp_f32_e32 v6, v6
	v_exp_f32_e32 v8, v8
	v_mul_f32_e32 v7, v143, v139

	v_fma_f32 v6, v6, s94, s94
	v_rcp_f32_e32 v6, v6
	v_fma_f32 v8, v8, s94, s94
	v_rcp_f32_e32 v8, v8
	v_mul_f32_e32 v10, 0xbab8aa3b, v132
	v_mul_f32_e32 v6, v7, v6
	v_mul_f32_e32 v7, v135, v131

	v_mul_f32_e32 v7, v7, v8
	v_mul_f32_e32 v8, 0xbab8aa3b, v140
	v_exp_f32_e32 v8, v8
	v_exp_f32_e32 v10, v10
	v_mul_f32_e32 v9, v144, v140

	v_fma_f32 v8, v8, s94, s94
	v_rcp_f32_e32 v8, v8
	v_fma_f32 v10, v10, s94, s94
	v_rcp_f32_e32 v10, v10
	v_mul_f32_e32 v12, 0xbab8aa3b, v133
	v_mul_f32_e32 v8, v9, v8
	v_mul_f32_e32 v9, v136, v132

	v_mul_f32_e32 v9, v9, v10
	v_mul_f32_e32 v10, 0xbab8aa3b, v141
	v_exp_f32_e32 v10, v10
	v_exp_f32_e32 v12, v12
	v_mul_f32_e32 v11, v145, v141

	v_fma_f32 v10, v10, s94, s94
	v_rcp_f32_e32 v10, v10
	v_fma_f32 v12, v12, s94, s94
	v_rcp_f32_e32 v12, v12
	v_med3_f32 v6, v6, s60, v195
	v_mul_f32_e32 v10, v11, v10
	v_mul_f32_e32 v11, v137, v133

	v_mul_f32_e32 v11, v11, v12
	v_med3_f32 v12, v4, s60, v195
	v_mov_b32_e32 v4, 0
	v_cvt_pk_fp8_f32 v4, v12, v6
	v_med3_f32 v6, v5, s60, v195
	v_med3_f32 v7, v7, s60, v195
	v_mov_b32_e32 v5, 0
	v_cvt_pk_fp8_f32 v5, v6, v7
	v_med3_f32 v8, v8, s60, v195
	v_med3_f32 v10, v10, s60, v195
	v_med3_f32 v6, v9, s60, v195
	v_med3_f32 v7, v11, s60, v195
	v_cvt_pk_fp8_f32 v4, v8, v10 op_sel:[0,0,1]
	v_cvt_pk_fp8_f32 v5, v6, v7 op_sel:[0,0,1]
	v_add_co_u32_e32 v6, vcc, s47, v2
	v_mul_f32_e32 v8, 0xbab8aa3b, v115
	s_nop 0
	v_addc_co_u32_e32 v7, vcc, 0, v3, vcc
	global_store_dwordx2 v[6:7], v[4:5], off
	v_mul_f32_e32 v4, 0xbab8aa3b, v122
	v_exp_f32_e32 v4, v4
	v_mul_f32_e32 v6, 0xbab8aa3b, v114
	v_exp_f32_e32 v6, v6
	v_mul_f32_e32 v5, v126, v122
	v_fma_f32 v4, v4, s94, s94
	v_rcp_f32_e32 v4, v4
	v_fma_f32 v6, v6, s94, s94
	v_rcp_f32_e32 v6, v6

	v_mul_f32_e32 v4, v5, v4
	v_mul_f32_e32 v5, v118, v114

	v_mul_f32_e32 v5, v5, v6
	v_mul_f32_e32 v6, 0xbab8aa3b, v123
	v_exp_f32_e32 v6, v6
	v_exp_f32_e32 v8, v8
	v_mul_f32_e32 v7, v127, v123

	v_fma_f32 v6, v6, s94, s94
	v_rcp_f32_e32 v6, v6
	v_fma_f32 v8, v8, s94, s94
	v_rcp_f32_e32 v8, v8
	v_mul_f32_e32 v10, 0xbab8aa3b, v116
	v_mul_f32_e32 v6, v7, v6
	v_mul_f32_e32 v7, v119, v115

	v_mul_f32_e32 v7, v7, v8
	v_mul_f32_e32 v8, 0xbab8aa3b, v124
	v_exp_f32_e32 v8, v8
	v_exp_f32_e32 v10, v10
	v_mul_f32_e32 v9, v128, v124

	v_fma_f32 v8, v8, s94, s94
	v_rcp_f32_e32 v8, v8
	v_fma_f32 v10, v10, s94, s94
	v_rcp_f32_e32 v10, v10
	v_mul_f32_e32 v12, 0xbab8aa3b, v117
	v_mul_f32_e32 v8, v9, v8
	v_mul_f32_e32 v9, v120, v116

	v_mul_f32_e32 v9, v9, v10
	v_mul_f32_e32 v10, 0xbab8aa3b, v125
	v_exp_f32_e32 v10, v10
	v_exp_f32_e32 v12, v12
	v_mul_f32_e32 v11, v129, v125

	v_fma_f32 v10, v10, s94, s94
	v_rcp_f32_e32 v10, v10
	v_fma_f32 v12, v12, s94, s94
	v_rcp_f32_e32 v12, v12
	v_med3_f32 v6, v6, s60, v195
	v_mul_f32_e32 v10, v11, v10
	v_mul_f32_e32 v11, v121, v117

	v_mul_f32_e32 v11, v11, v12
	v_med3_f32 v12, v4, s60, v195
	v_mov_b32_e32 v4, 0
	v_cvt_pk_fp8_f32 v4, v12, v6
	v_med3_f32 v6, v5, s60, v195
	v_med3_f32 v7, v7, s60, v195
	v_mov_b32_e32 v5, 0
	v_cvt_pk_fp8_f32 v5, v6, v7
	v_med3_f32 v8, v8, s60, v195
	v_med3_f32 v10, v10, s60, v195
	v_med3_f32 v6, v9, s60, v195
	v_med3_f32 v7, v11, s60, v195
	v_cvt_pk_fp8_f32 v4, v8, v10 op_sel:[0,0,1]
	v_cvt_pk_fp8_f32 v5, v6, v7 op_sel:[0,0,1]
	v_add_co_u32_e32 v6, vcc, s48, v2
	v_mul_f32_e32 v8, 0xbab8aa3b, v103
	s_nop 0
	v_addc_co_u32_e32 v7, vcc, 0, v3, vcc
	global_store_dwordx2 v[6:7], v[4:5], off
	v_mul_f32_e32 v4, 0xbab8aa3b, v110
	v_exp_f32_e32 v4, v4
	v_mul_f32_e32 v6, 0xbab8aa3b, v102
	v_exp_f32_e32 v6, v6
	v_mul_f32_e32 v5, v106, v110
	v_fma_f32 v4, v4, s94, s94
	v_rcp_f32_e32 v4, v4
	v_fma_f32 v6, v6, s94, s94
	v_rcp_f32_e32 v6, v6

	v_mul_f32_e32 v4, v5, v4
	v_mul_f32_e32 v5, v98, v102

	v_mul_f32_e32 v5, v5, v6
	v_mul_f32_e32 v6, 0xbab8aa3b, v111
	v_exp_f32_e32 v6, v6
	v_exp_f32_e32 v8, v8
	v_mul_f32_e32 v7, v107, v111

	v_fma_f32 v6, v6, s94, s94
	v_rcp_f32_e32 v6, v6
	v_fma_f32 v8, v8, s94, s94
	v_rcp_f32_e32 v8, v8
	v_mul_f32_e32 v10, 0xbab8aa3b, v104
	v_mul_f32_e32 v6, v7, v6
	v_mul_f32_e32 v7, v99, v103

	v_mul_f32_e32 v7, v7, v8
	v_mul_f32_e32 v8, 0xbab8aa3b, v112
	v_exp_f32_e32 v8, v8
	v_exp_f32_e32 v10, v10
	v_mul_f32_e32 v9, v108, v112

	v_fma_f32 v8, v8, s94, s94
	v_rcp_f32_e32 v8, v8
	v_fma_f32 v10, v10, s94, s94
	v_rcp_f32_e32 v10, v10
	v_mul_f32_e32 v12, 0xbab8aa3b, v105
	v_mul_f32_e32 v8, v9, v8
	v_mul_f32_e32 v9, v100, v104

	v_mul_f32_e32 v9, v9, v10
	v_mul_f32_e32 v10, 0xbab8aa3b, v113
	v_exp_f32_e32 v10, v10
	v_exp_f32_e32 v12, v12
	v_mul_f32_e32 v11, v109, v113

	v_fma_f32 v10, v10, s94, s94
	v_rcp_f32_e32 v10, v10
	v_fma_f32 v12, v12, s94, s94
	v_rcp_f32_e32 v12, v12
	v_med3_f32 v6, v6, s60, v195
	v_mul_f32_e32 v10, v11, v10
	v_mul_f32_e32 v11, v101, v105

	v_mul_f32_e32 v11, v11, v12
	v_med3_f32 v12, v4, s60, v195
	v_mov_b32_e32 v4, 0
	v_cvt_pk_fp8_f32 v4, v12, v6
	v_med3_f32 v6, v5, s60, v195
	v_med3_f32 v7, v7, s60, v195
	v_mov_b32_e32 v5, 0
	v_cvt_pk_fp8_f32 v5, v6, v7
	v_med3_f32 v8, v8, s60, v195
	v_med3_f32 v10, v10, s60, v195
	v_med3_f32 v6, v9, s60, v195
	v_med3_f32 v7, v11, s60, v195
	v_cvt_pk_fp8_f32 v4, v8, v10 op_sel:[0,0,1]
	v_cvt_pk_fp8_f32 v5, v6, v7 op_sel:[0,0,1]
	s_mov_b32 s2, 0x10000
	v_add_co_u32_e32 v6, vcc, s2, v2
	v_mul_f32_e32 v8, 0xbab8aa3b, v87
	s_nop 0
	v_addc_co_u32_e32 v7, vcc, 0, v3, vcc
	global_store_dwordx2 v[6:7], v[4:5], off
	v_mul_f32_e32 v4, 0xbab8aa3b, v94
	v_exp_f32_e32 v4, v4
	v_mul_f32_e32 v6, 0xbab8aa3b, v86
	v_exp_f32_e32 v6, v6
	v_mul_f32_e32 v5, v90, v94
	v_fma_f32 v4, v4, s94, s94
	v_rcp_f32_e32 v4, v4
	v_fma_f32 v6, v6, s94, s94
	v_rcp_f32_e32 v6, v6

	v_mul_f32_e32 v4, v5, v4
	v_mul_f32_e32 v5, v82, v86

	v_mul_f32_e32 v5, v5, v6
	v_mul_f32_e32 v6, 0xbab8aa3b, v95
	v_exp_f32_e32 v6, v6
	v_exp_f32_e32 v8, v8
	v_mul_f32_e32 v7, v91, v95

	v_fma_f32 v6, v6, s94, s94
	v_rcp_f32_e32 v6, v6
	v_fma_f32 v8, v8, s94, s94
	v_rcp_f32_e32 v8, v8
	v_mul_f32_e32 v10, 0xbab8aa3b, v88
	v_mul_f32_e32 v6, v7, v6
	v_mul_f32_e32 v7, v83, v87

	v_mul_f32_e32 v7, v7, v8
	v_mul_f32_e32 v8, 0xbab8aa3b, v96
	v_exp_f32_e32 v8, v8
	v_exp_f32_e32 v10, v10
	v_mul_f32_e32 v9, v92, v96

	v_fma_f32 v8, v8, s94, s94
	v_rcp_f32_e32 v8, v8
	v_fma_f32 v10, v10, s94, s94
	v_rcp_f32_e32 v10, v10
	v_mul_f32_e32 v12, 0xbab8aa3b, v89
	v_mul_f32_e32 v8, v9, v8
	v_mul_f32_e32 v9, v84, v88

	v_mul_f32_e32 v9, v9, v10
	v_mul_f32_e32 v10, 0xbab8aa3b, v97
	v_exp_f32_e32 v10, v10
	v_exp_f32_e32 v12, v12
	v_mul_f32_e32 v11, v93, v97

	v_fma_f32 v10, v10, s94, s94
	v_rcp_f32_e32 v10, v10
	v_fma_f32 v12, v12, s94, s94
	v_rcp_f32_e32 v12, v12
	v_med3_f32 v6, v6, s60, v195
	v_mul_f32_e32 v10, v11, v10
	v_mul_f32_e32 v11, v85, v89

	v_mul_f32_e32 v11, v11, v12
	v_med3_f32 v12, v4, s60, v195
	v_mov_b32_e32 v4, 0
	v_cvt_pk_fp8_f32 v4, v12, v6
	v_med3_f32 v6, v5, s60, v195
	v_med3_f32 v7, v7, s60, v195
	v_mov_b32_e32 v5, 0
	v_cvt_pk_fp8_f32 v5, v6, v7
	v_med3_f32 v8, v8, s60, v195
	v_med3_f32 v10, v10, s60, v195
	v_med3_f32 v6, v9, s60, v195
	v_med3_f32 v7, v11, s60, v195
	v_cvt_pk_fp8_f32 v4, v8, v10 op_sel:[0,0,1]
	v_cvt_pk_fp8_f32 v5, v6, v7 op_sel:[0,0,1]
	v_add_co_u32_e32 v6, vcc, s44, v2
	v_mul_f32_e32 v8, 0xbab8aa3b, v71
	s_nop 0
	v_addc_co_u32_e32 v7, vcc, 0, v3, vcc
	global_store_dwordx2 v[6:7], v[4:5], off
	v_mul_f32_e32 v4, 0xbab8aa3b, v78
	v_exp_f32_e32 v4, v4
	v_mul_f32_e32 v6, 0xbab8aa3b, v70
	v_exp_f32_e32 v6, v6
	v_mul_f32_e32 v5, v74, v78
	v_fma_f32 v4, v4, s94, s94
	v_rcp_f32_e32 v4, v4
	v_fma_f32 v6, v6, s94, s94
	v_rcp_f32_e32 v6, v6

	v_mul_f32_e32 v4, v5, v4
	v_mul_f32_e32 v5, v66, v70

	v_mul_f32_e32 v5, v5, v6
	v_mul_f32_e32 v6, 0xbab8aa3b, v79
	v_exp_f32_e32 v6, v6
	v_exp_f32_e32 v8, v8
	v_mul_f32_e32 v7, v75, v79

	v_fma_f32 v6, v6, s94, s94
	v_rcp_f32_e32 v6, v6
	v_fma_f32 v8, v8, s94, s94
	v_rcp_f32_e32 v8, v8
	v_mul_f32_e32 v10, 0xbab8aa3b, v72
	v_mul_f32_e32 v6, v7, v6
	v_mul_f32_e32 v7, v67, v71

	v_mul_f32_e32 v7, v7, v8
	v_mul_f32_e32 v8, 0xbab8aa3b, v80
	v_exp_f32_e32 v8, v8
	v_exp_f32_e32 v10, v10
	v_mul_f32_e32 v9, v76, v80

	v_fma_f32 v8, v8, s94, s94
	v_rcp_f32_e32 v8, v8
	v_fma_f32 v10, v10, s94, s94
	v_rcp_f32_e32 v10, v10
	v_mul_f32_e32 v12, 0xbab8aa3b, v73
	v_mul_f32_e32 v8, v9, v8
	v_mul_f32_e32 v9, v68, v72

	v_mul_f32_e32 v9, v9, v10
	v_mul_f32_e32 v10, 0xbab8aa3b, v81
	v_exp_f32_e32 v10, v10
	v_exp_f32_e32 v12, v12
	v_mul_f32_e32 v11, v77, v81

	v_fma_f32 v10, v10, s94, s94
	v_rcp_f32_e32 v10, v10
	v_fma_f32 v12, v12, s94, s94
	v_rcp_f32_e32 v12, v12
	v_med3_f32 v6, v6, s60, v195
	v_mul_f32_e32 v10, v11, v10
	v_mul_f32_e32 v11, v69, v73

	v_mul_f32_e32 v11, v11, v12
	v_med3_f32 v12, v4, s60, v195
	v_mov_b32_e32 v4, 0
	v_cvt_pk_fp8_f32 v4, v12, v6
	v_med3_f32 v6, v5, s60, v195
	v_med3_f32 v7, v7, s60, v195
	v_mov_b32_e32 v5, 0
	v_cvt_pk_fp8_f32 v5, v6, v7
	v_med3_f32 v8, v8, s60, v195
	v_med3_f32 v10, v10, s60, v195
	v_med3_f32 v6, v9, s60, v195
	v_med3_f32 v7, v11, s60, v195
	v_cvt_pk_fp8_f32 v4, v8, v10 op_sel:[0,0,1]
	v_cvt_pk_fp8_f32 v5, v6, v7 op_sel:[0,0,1]
	v_add_co_u32_e32 v6, vcc, s46, v2
	v_mul_f32_e32 v8, 0xbab8aa3b, v55
	s_nop 0
	v_addc_co_u32_e32 v7, vcc, 0, v3, vcc
	global_store_dwordx2 v[6:7], v[4:5], off
	v_mul_f32_e32 v4, 0xbab8aa3b, v62
	v_exp_f32_e32 v4, v4
	v_mul_f32_e32 v6, 0xbab8aa3b, v54
	v_exp_f32_e32 v6, v6
	v_mul_f32_e32 v5, v58, v62
	v_fma_f32 v4, v4, s94, s94
	v_rcp_f32_e32 v4, v4
	v_fma_f32 v6, v6, s94, s94
	v_rcp_f32_e32 v6, v6

	v_mul_f32_e32 v4, v5, v4
	v_mul_f32_e32 v5, v50, v54

	v_mul_f32_e32 v5, v5, v6
	v_mul_f32_e32 v6, 0xbab8aa3b, v63
	v_exp_f32_e32 v6, v6
	v_exp_f32_e32 v8, v8
	v_mul_f32_e32 v7, v59, v63

	v_fma_f32 v6, v6, s94, s94
	v_rcp_f32_e32 v6, v6
	v_fma_f32 v8, v8, s94, s94
	v_rcp_f32_e32 v8, v8
	v_mul_f32_e32 v10, 0xbab8aa3b, v56
	v_mul_f32_e32 v6, v7, v6
	v_mul_f32_e32 v7, v51, v55

	v_mul_f32_e32 v7, v7, v8
	v_mul_f32_e32 v8, 0xbab8aa3b, v64
	v_exp_f32_e32 v8, v8
	v_exp_f32_e32 v10, v10
	v_mul_f32_e32 v9, v60, v64

	v_fma_f32 v8, v8, s94, s94
	v_rcp_f32_e32 v8, v8
	v_fma_f32 v10, v10, s94, s94
	v_rcp_f32_e32 v10, v10
	v_mul_f32_e32 v12, 0xbab8aa3b, v57
	v_mul_f32_e32 v8, v9, v8
	v_mul_f32_e32 v9, v52, v56

	v_mul_f32_e32 v9, v9, v10
	v_mul_f32_e32 v10, 0xbab8aa3b, v65
	v_exp_f32_e32 v10, v10
	v_exp_f32_e32 v12, v12
	v_mul_f32_e32 v11, v61, v65

	v_fma_f32 v10, v10, s94, s94
	v_rcp_f32_e32 v10, v10
	v_fma_f32 v12, v12, s94, s94
	v_rcp_f32_e32 v12, v12
	v_med3_f32 v6, v6, s60, v195
	v_mul_f32_e32 v10, v11, v10
	v_mul_f32_e32 v11, v53, v57

	v_mul_f32_e32 v11, v11, v12
	v_med3_f32 v12, v4, s60, v195
	v_mov_b32_e32 v4, 0
	v_cvt_pk_fp8_f32 v4, v12, v6
	v_med3_f32 v6, v5, s60, v195
	v_med3_f32 v7, v7, s60, v195
	v_mov_b32_e32 v5, 0
	v_cvt_pk_fp8_f32 v5, v6, v7
	v_med3_f32 v8, v8, s60, v195
	v_med3_f32 v10, v10, s60, v195
	v_med3_f32 v6, v9, s60, v195
	v_med3_f32 v7, v11, s60, v195
	v_cvt_pk_fp8_f32 v4, v8, v10 op_sel:[0,0,1]
	v_cvt_pk_fp8_f32 v5, v6, v7 op_sel:[0,0,1]
	v_add_co_u32_e32 v2, vcc, 0x16000, v2
	s_xor_b64 s[0:1], s[28:29], -1
	s_nop 0
	v_addc_co_u32_e32 v3, vcc, 0, v3, vcc
	v_writelane_b32 v254, s62, 11
	s_and_b64 vcc, exec, s[0:1]
	v_writelane_b32 v254, s68, 10
	s_mov_b32 s70, s69
	global_store_dwordx2 v[2:3], v[4:5], off
	s_cbranch_vccnz .LBB0_1847
